# P7 epilogue: the read-once residual loads marked non-temporal (lower load latency in a latency-bound ring)
# baseline (speedup 1.0000x reference)
; __device__ __forceinline__ unsigned cvt_pk_bf16(float lo, float hi) { unsigned r; asm volatile("v_cvt_pk_bf16_f32 %0, %1, %2" : "=v"(r) : "v"(lo), "v"(hi)); return r; }
; __device__ __forceinline__ unsigned cvt_pk4_fp8(float a, float b, float c, float d) { int w; asm("" : "=v"(w));     w = __builtin_amdgcn_cvt_pk_fp8_f32(a, b, w, false); w = __builtin_amdgcn_cvt_pk_fp8_f32(c, d, w, true); return (unsigned)w; }
;     __device__ __forceinline__ void operator()(const f32x4 (&acc)[2][2][4][2], const Unit& u, int wr, int wc, int fr, int fq) const {
;         const int row0 = u.pm * BM + wr * 64 + fr, col0 = u.pn * BM + wc * 32 + 8 * fq;
;         f32x4 gv[2][2];
; #pragma unroll
;         for (int bj = 0; bj < 2; ++bj)
; #pragma unroll
;             for (int n = 0; n < 2; ++n) gv[bj][n] = *(const f32x4*)(g + col0 + bj * HALF + 4 * n);
; #pragma unroll
;         for (int ai = 0; ai < 2; ++ai)
; #pragma unroll
;             for (int m = 0; m < 4; ++m) { const size_t off = (size_t)(row0 + ai * HALF + m * 16) * DM + col0;
; #pragma unroll
;                 for (int bj = 0; bj < 2; ++bj) { const f32x4 v0 = *(const f32x4*)(base + off + bj * HALF) + acc[ai][bj][m][0], v1 = *(const f32x4*)(base + off + bj * HALF + 4) + acc[ai][bj][m][1];
;                     { u32x4 xw; xw.x = cvt_pk_bf16(v0[0], v0[1]); xw.y = cvt_pk_bf16(v0[2], v0[3]); xw.z = cvt_pk_bf16(v1[0], v1[1]); xw.w = cvt_pk_bf16(v1[2], v1[3]); *(u32x4*)(C + off + bj * HALF) = xw; }
;                     const f32x4 h0 = v0 * gv[bj][0], h1 = v1 * gv[bj][1];
;                     u32x2 w; w.x = cvt_pk4_fp8(h0[0], h0[1], h0[2], h0[3]); w.y = cvt_pk4_fp8(h1[0], h1[1], h1[2], h1[3]);
;                     *(u32x2*)(H2 + off + bj * HALF) = w; } }
.LBB0_921:
	s_lshl_b32 s36, s52, 8
	v_mbcnt_lo_u32_b32 v96, -1, 0
	v_mbcnt_hi_u32_b32 v96, -1, v96
	s_add_i32 s36, s36, s34
	s_lshl_b32 s35, s35, 8
	v_ashrrev_i32_e32 v97, 1, v96
	s_or_b32 s35, s35, s84
	v_and_b32_e32 v97, -8, v97
	v_and_or_b32 v144, v96, 15, s36
	v_add_u32_e32 v148, s35, v97
	v_ashrrev_i32_e32 v145, 31, v144
	v_ashrrev_i32_e32 v149, 31, v148
	v_lshlrev_b64 v[96:97], 11, v[144:145]
	v_lshl_add_u64 v[146:147], v[96:97], 0, v[148:149]
	v_lshl_add_u64 v[168:169], v[146:147], 2, s[6:7]
	global_load_dwordx4 v[160:163], v[168:169], off
	global_load_dwordx4 v[164:167], v[168:169], off offset:16
	v_lshl_add_u64 v[100:101], v[148:149], 2, s[12:13]
	global_load_dwordx4 v[116:119], v[100:101], off
	global_load_dwordx4 v[112:115], v[100:101], off offset:16
	global_load_dwordx4 v[96:99], v[100:101], off offset:528
	s_nop 0
	global_load_dwordx4 v[100:103], v[100:101], off offset:512
	v_lshlrev_b32_e32 v232, 2, v146
	global_load_dwordx4 v[176:179], v232, s[6:7] offset:512 nt
	global_load_dwordx4 v[180:183], v232, s[6:7] offset:528 nt
	v_add_u32_e32 v233, 0x20000, v232
	global_load_dwordx4 v[184:187], v233, s[6:7] nt
	global_load_dwordx4 v[188:191], v233, s[6:7] offset:16 nt
	v_add_u32_e32 v233, 0x20000, v232
	global_load_dwordx4 v[192:195], v233, s[6:7] offset:512 nt
	global_load_dwordx4 v[196:199], v233, s[6:7] offset:528 nt
	v_add_u32_e32 v233, 0x40000, v232
	global_load_dwordx4 v[200:203], v233, s[6:7] nt
	global_load_dwordx4 v[204:207], v233, s[6:7] offset:16 nt
	v_add_u32_e32 v233, 0x40000, v232
	global_load_dwordx4 v[208:211], v233, s[6:7] offset:512 nt
	global_load_dwordx4 v[212:215], v233, s[6:7] offset:528 nt
	v_add_u32_e32 v233, 0x60000, v232
	global_load_dwordx4 v[216:219], v233, s[6:7] nt
	global_load_dwordx4 v[220:223], v233, s[6:7] offset:16 nt
	v_add_u32_e32 v233, 0x60000, v232
	global_load_dwordx4 v[224:227], v233, s[6:7] offset:512 nt
	global_load_dwordx4 v[228:231], v233, s[6:7] offset:528 nt
	v_lshl_add_u64 v[172:173], v[146:147], 1, s[14:15]
	v_lshl_add_u64 v[174:175], s[10:11], 0, v[146:147]
	s_andn2_b64 vcc, exec, s[50:51]
	s_mov_b64 s[50:51], -1
	s_waitcnt vmcnt(19)
	v_pk_add_f32 v[140:141], v[140:141], v[160:161]
	s_waitcnt vmcnt(18)
	v_pk_add_f32 v[160:161], v[138:139], v[166:167]
	v_pk_add_f32 v[138:139], v[136:137], v[164:165]
	v_pk_add_f32 v[142:143], v[142:143], v[162:163]
	v_cvt_pk_bf16_f32 v136, v140, v141
	s_waitcnt vmcnt(17)
	v_pk_mul_f32 v[140:141], v[116:117], v[140:141]
	s_waitcnt vmcnt(16)
	v_pk_mul_f32 v[162:163], v[112:113], v[138:139]
	v_cvt_pk_fp8_f32 v170, v140, v141
	v_cvt_pk_fp8_f32 v171, v162, v163
	v_cvt_pk_bf16_f32 v137, v142, v143
	v_pk_mul_f32 v[140:141], v[118:119], v[142:143]
	v_pk_mul_f32 v[142:143], v[114:115], v[160:161]
	v_cvt_pk_fp8_f32 v170, v140, v141 op_sel:[0,0,1]
	v_cvt_pk_fp8_f32 v171, v142, v143 op_sel:[0,0,1]
	v_cvt_pk_bf16_f32 v138, v138, v139
	v_cvt_pk_bf16_f32 v139, v160, v161
	global_store_dwordx4 v[172:173], v[136:139], off
	global_store_dwordx2 v[174:175], v[170:171], off
	v_or_b32_e32 v162, 16, v144
	v_ashrrev_i32_e32 v163, 31, v162
	v_lshlrev_b64 v[162:163], 11, v[162:163]
	v_lshl_add_u64 v[162:163], v[162:163], 0, v[148:149]
	v_lshl_add_u64 v[164:165], v[162:163], 2, s[6:7]
	s_waitcnt vmcnt(14)
	v_pk_add_f32 v[132:133], v[132:133], v[176:177]
	v_pk_add_f32 v[136:137], v[130:131], v[182:183]
	v_pk_add_f32 v[130:131], v[128:129], v[180:181]
	v_pk_add_f32 v[134:135], v[134:135], v[178:179]
	v_add_u32_e32 v233, 0x100000, v232
	global_load_dwordx4 v[176:179], v233, s[6:7] nt
	global_load_dwordx4 v[180:183], v233, s[6:7] offset:16 nt
	v_cvt_pk_bf16_f32 v128, v132, v133
	v_pk_mul_f32 v[132:133], v[100:101], v[132:133]
	v_pk_mul_f32 v[138:139], v[96:97], v[130:131]
	v_cvt_pk_fp8_f32 v160, v132, v133
	v_cvt_pk_fp8_f32 v161, v138, v139
	v_cvt_pk_bf16_f32 v129, v134, v135
	v_pk_mul_f32 v[132:133], v[102:103], v[134:135]
	v_pk_mul_f32 v[134:135], v[98:99], v[136:137]
	v_cvt_pk_fp8_f32 v160, v132, v133 op_sel:[0,0,1]
	v_cvt_pk_fp8_f32 v161, v134, v135 op_sel:[0,0,1]
	v_cvt_pk_bf16_f32 v130, v130, v131
	v_cvt_pk_bf16_f32 v131, v136, v137
	global_store_dwordx4 v[172:173], v[128:131], off offset:256
	global_store_dwordx2 v[174:175], v[160:161], off offset:128
	v_lshl_add_u64 v[138:139], v[162:163], 1, s[14:15]
	v_lshl_add_u64 v[140:141], s[10:11], 0, v[162:163]
	s_waitcnt vmcnt(16)
	v_pk_add_f32 v[124:125], v[124:125], v[184:185]
	v_pk_add_f32 v[128:129], v[122:123], v[190:191]
	v_pk_add_f32 v[122:123], v[120:121], v[188:189]
	v_pk_add_f32 v[126:127], v[126:127], v[186:187]
	v_add_u32_e32 v233, 0x100000, v232
	global_load_dwordx4 v[184:187], v233, s[6:7] offset:512 nt
	global_load_dwordx4 v[188:191], v233, s[6:7] offset:528 nt
	v_cvt_pk_bf16_f32 v120, v124, v125
	v_pk_mul_f32 v[124:125], v[116:117], v[124:125]
	v_pk_mul_f32 v[130:131], v[112:113], v[122:123]
	v_cvt_pk_fp8_f32 v136, v124, v125
	v_cvt_pk_fp8_f32 v137, v130, v131
	v_cvt_pk_bf16_f32 v121, v126, v127
	v_pk_mul_f32 v[124:125], v[118:119], v[126:127]
	v_pk_mul_f32 v[126:127], v[114:115], v[128:129]
	v_cvt_pk_fp8_f32 v136, v124, v125 op_sel:[0,0,1]
	v_cvt_pk_fp8_f32 v137, v126, v127 op_sel:[0,0,1]
	v_cvt_pk_bf16_f32 v122, v122, v123
	v_cvt_pk_bf16_f32 v123, v128, v129
	global_store_dwordx4 v[138:139], v[120:123], off
	global_store_dwordx2 v[140:141], v[136:137], off
	v_or_b32_e32 v130, 32, v144
	v_ashrrev_i32_e32 v131, 31, v130
	v_lshlrev_b64 v[130:131], 11, v[130:131]
	v_lshl_add_u64 v[130:131], v[130:131], 0, v[148:149]
	v_lshl_add_u64 v[132:133], v[130:131], 2, s[6:7]
	s_waitcnt vmcnt(18)
; __device__ __forceinline__ unsigned cvt_pk_bf16(float lo, float hi) { unsigned r; asm volatile("v_cvt_pk_bf16_f32 %0, %1, %2" : "=v"(r) : "v"(lo), "v"(hi)); return r; }
; __device__ __forceinline__ unsigned cvt_pk4_fp8(float a, float b, float c, float d) { int w; asm("" : "=v"(w));     w = __builtin_amdgcn_cvt_pk_fp8_f32(a, b, w, false); w = __builtin_amdgcn_cvt_pk_fp8_f32(c, d, w, true); return (unsigned)w; }
;     __device__ __forceinline__ void operator()(const f32x4 (&acc)[2][2][4][2], const Unit& u, int wr, int wc, int fr, int fq) const {
;     ...
;         for (int ai = 0; ai < 2; ++ai)
; #pragma unroll
;             for (int m = 0; m < 4; ++m) { const size_t off = (size_t)(row0 + ai * HALF + m * 16) * DM + col0;
; #pragma unroll
;                 for (int bj = 0; bj < 2; ++bj) { const f32x4 v0 = *(const f32x4*)(base + off + bj * HALF) + acc[ai][bj][m][0], v1 = *(const f32x4*)(base + off + bj * HALF + 4) + acc[ai][bj][m][1];
;                     { u32x4 xw; xw.x = cvt_pk_bf16(v0[0], v0[1]); xw.y = cvt_pk_bf16(v0[2], v0[3]); xw.z = cvt_pk_bf16(v1[0], v1[1]); xw.w = cvt_pk_bf16(v1[2], v1[3]); *(u32x4*)(C + off + bj * HALF) = xw; }
;                     const f32x4 h0 = v0 * gv[bj][0], h1 = v1 * gv[bj][1];
;                     u32x2 w; w.x = cvt_pk4_fp8(h0[0], h0[1], h0[2], h0[3]); w.y = cvt_pk4_fp8(h1[0], h1[1], h1[2], h1[3]);
;                     *(u32x2*)(H2 + off + bj * HALF) = w; } }
	v_pk_add_f32 v[108:109], v[108:109], v[192:193]
	v_pk_add_f32 v[120:121], v[106:107], v[198:199]
	v_pk_add_f32 v[106:107], v[104:105], v[196:197]
	v_pk_add_f32 v[110:111], v[110:111], v[194:195]
	v_add_u32_e32 v233, 0x120000, v232
	global_load_dwordx4 v[192:195], v233, s[6:7] nt
	global_load_dwordx4 v[196:199], v233, s[6:7] offset:16 nt
	v_cvt_pk_bf16_f32 v104, v108, v109
	v_pk_mul_f32 v[108:109], v[100:101], v[108:109]
	v_pk_mul_f32 v[122:123], v[96:97], v[106:107]
	v_cvt_pk_fp8_f32 v128, v108, v109
	v_cvt_pk_fp8_f32 v129, v122, v123
	v_cvt_pk_bf16_f32 v105, v110, v111
	v_pk_mul_f32 v[108:109], v[102:103], v[110:111]
	v_pk_mul_f32 v[110:111], v[98:99], v[120:121]
	v_cvt_pk_fp8_f32 v128, v108, v109 op_sel:[0,0,1]
	v_cvt_pk_fp8_f32 v129, v110, v111 op_sel:[0,0,1]
	v_cvt_pk_bf16_f32 v106, v106, v107
	v_cvt_pk_bf16_f32 v107, v120, v121
	global_store_dwordx4 v[138:139], v[104:107], off offset:256
	global_store_dwordx2 v[140:141], v[128:129], off offset:128
	v_lshl_add_u64 v[122:123], v[130:131], 1, s[14:15]
	v_lshl_add_u64 v[124:125], s[10:11], 0, v[130:131]
	s_waitcnt vmcnt(20)
	v_pk_add_f32 v[92:93], v[92:93], v[200:201]
	v_pk_add_f32 v[104:105], v[90:91], v[206:207]
	v_pk_add_f32 v[90:91], v[88:89], v[204:205]
	v_pk_add_f32 v[94:95], v[94:95], v[202:203]
	v_add_u32_e32 v233, 0x120000, v232
	global_load_dwordx4 v[200:203], v233, s[6:7] offset:512 nt
	global_load_dwordx4 v[204:207], v233, s[6:7] offset:528 nt
	v_cvt_pk_bf16_f32 v88, v92, v93
	v_pk_mul_f32 v[92:93], v[116:117], v[92:93]
	v_pk_mul_f32 v[106:107], v[112:113], v[90:91]
	v_cvt_pk_fp8_f32 v120, v92, v93
	v_cvt_pk_fp8_f32 v121, v106, v107
	v_cvt_pk_bf16_f32 v89, v94, v95
	v_pk_mul_f32 v[92:93], v[118:119], v[94:95]
	v_pk_mul_f32 v[94:95], v[114:115], v[104:105]
	v_cvt_pk_fp8_f32 v120, v92, v93 op_sel:[0,0,1]
	v_cvt_pk_fp8_f32 v121, v94, v95 op_sel:[0,0,1]
	v_cvt_pk_bf16_f32 v90, v90, v91
	v_cvt_pk_bf16_f32 v91, v104, v105
	global_store_dwordx4 v[122:123], v[88:91], off
	global_store_dwordx2 v[124:125], v[120:121], off
	v_or_b32_e32 v106, 48, v144
	v_ashrrev_i32_e32 v107, 31, v106
	v_lshlrev_b64 v[106:107], 11, v[106:107]
	v_lshl_add_u64 v[106:107], v[106:107], 0, v[148:149]
	v_lshl_add_u64 v[108:109], v[106:107], 2, s[6:7]
	s_waitcnt vmcnt(22)
	v_pk_add_f32 v[84:85], v[84:85], v[208:209]
	v_pk_add_f32 v[88:89], v[82:83], v[214:215]
	v_pk_add_f32 v[82:83], v[80:81], v[212:213]
	v_pk_add_f32 v[86:87], v[86:87], v[210:211]
	v_add_u32_e32 v233, 0x140000, v232
	global_load_dwordx4 v[208:211], v233, s[6:7] nt
	global_load_dwordx4 v[212:215], v233, s[6:7] offset:16 nt
	v_cvt_pk_bf16_f32 v80, v84, v85
	v_pk_mul_f32 v[84:85], v[100:101], v[84:85]
	v_pk_mul_f32 v[90:91], v[96:97], v[82:83]
	v_cvt_pk_fp8_f32 v104, v84, v85
	v_cvt_pk_fp8_f32 v105, v90, v91
	v_cvt_pk_bf16_f32 v81, v86, v87
	v_pk_mul_f32 v[84:85], v[102:103], v[86:87]
	v_pk_mul_f32 v[86:87], v[98:99], v[88:89]
	v_cvt_pk_fp8_f32 v104, v84, v85 op_sel:[0,0,1]
	v_cvt_pk_fp8_f32 v105, v86, v87 op_sel:[0,0,1]
	v_cvt_pk_bf16_f32 v82, v82, v83
	v_cvt_pk_bf16_f32 v83, v88, v89
	global_store_dwordx4 v[122:123], v[80:83], off offset:256
	global_store_dwordx2 v[124:125], v[104:105], off offset:128
	v_lshl_add_u64 v[90:91], v[106:107], 1, s[14:15]
	v_lshl_add_u64 v[92:93], s[10:11], 0, v[106:107]
	s_waitcnt vmcnt(24)
	v_pk_add_f32 v[76:77], v[76:77], v[216:217]
	v_pk_add_f32 v[80:81], v[74:75], v[222:223]
	v_pk_add_f32 v[74:75], v[72:73], v[220:221]
	v_pk_add_f32 v[78:79], v[78:79], v[218:219]
	v_add_u32_e32 v233, 0x140000, v232
	global_load_dwordx4 v[216:219], v233, s[6:7] offset:512 nt
	global_load_dwordx4 v[220:223], v233, s[6:7] offset:528 nt
	v_cvt_pk_bf16_f32 v72, v76, v77
	v_pk_mul_f32 v[76:77], v[116:117], v[76:77]
	v_pk_mul_f32 v[82:83], v[112:113], v[74:75]
	v_cvt_pk_fp8_f32 v88, v76, v77
	v_cvt_pk_fp8_f32 v89, v82, v83
	v_cvt_pk_bf16_f32 v73, v78, v79
	v_pk_mul_f32 v[76:77], v[118:119], v[78:79]
	v_pk_mul_f32 v[78:79], v[114:115], v[80:81]
	v_cvt_pk_fp8_f32 v88, v76, v77 op_sel:[0,0,1]
	v_cvt_pk_fp8_f32 v89, v78, v79 op_sel:[0,0,1]
	v_cvt_pk_bf16_f32 v74, v74, v75
	v_cvt_pk_bf16_f32 v75, v80, v81
	global_store_dwordx4 v[90:91], v[72:75], off
	global_store_dwordx2 v[92:93], v[88:89], off
	v_lshl_add_u64 v[82:83], v[146:147], 0, s[20:21]
	v_lshl_add_u64 v[84:85], v[82:83], 2, s[6:7]
	s_waitcnt vmcnt(26)
	v_pk_add_f32 v[68:69], v[68:69], v[224:225]
	v_pk_add_f32 v[72:73], v[66:67], v[230:231]
	v_pk_add_f32 v[66:67], v[64:65], v[228:229]
	v_pk_add_f32 v[70:71], v[70:71], v[226:227]
	v_add_u32_e32 v233, 0x160000, v232
	global_load_dwordx4 v[224:227], v233, s[6:7] nt
	global_load_dwordx4 v[228:231], v233, s[6:7] offset:16 nt
	v_cvt_pk_bf16_f32 v64, v68, v69
	v_pk_mul_f32 v[68:69], v[100:101], v[68:69]
	v_pk_mul_f32 v[74:75], v[96:97], v[66:67]
	v_cvt_pk_fp8_f32 v80, v68, v69
	v_cvt_pk_fp8_f32 v81, v74, v75
	v_cvt_pk_bf16_f32 v65, v70, v71
	v_pk_mul_f32 v[68:69], v[102:103], v[70:71]
	v_pk_mul_f32 v[70:71], v[98:99], v[72:73]
	v_cvt_pk_fp8_f32 v80, v68, v69 op_sel:[0,0,1]
	v_cvt_pk_fp8_f32 v81, v70, v71 op_sel:[0,0,1]
	v_cvt_pk_bf16_f32 v66, v66, v67
	v_cvt_pk_bf16_f32 v67, v72, v73
	global_store_dwordx4 v[90:91], v[64:67], off offset:256
	global_store_dwordx2 v[92:93], v[80:81], off offset:128
	v_lshl_add_u64 v[74:75], v[82:83], 1, s[14:15]
	v_lshl_add_u64 v[76:77], s[10:11], 0, v[82:83]
	s_waitcnt vmcnt(26)
; __device__ __forceinline__ unsigned cvt_pk_bf16(float lo, float hi) { unsigned r; asm volatile("v_cvt_pk_bf16_f32 %0, %1, %2" : "=v"(r) : "v"(lo), "v"(hi)); return r; }
; __device__ __forceinline__ unsigned cvt_pk4_fp8(float a, float b, float c, float d) { int w; asm("" : "=v"(w));     w = __builtin_amdgcn_cvt_pk_fp8_f32(a, b, w, false); w = __builtin_amdgcn_cvt_pk_fp8_f32(c, d, w, true); return (unsigned)w; }
;     __device__ __forceinline__ void operator()(const f32x4 (&acc)[2][2][4][2], const Unit& u, int wr, int wc, int fr, int fq) const {
;     ...
;             for (int m = 0; m < 4; ++m) { const size_t off = (size_t)(row0 + ai * HALF + m * 16) * DM + col0;
; #pragma unroll
;                 for (int bj = 0; bj < 2; ++bj) { const f32x4 v0 = *(const f32x4*)(base + off + bj * HALF) + acc[ai][bj][m][0], v1 = *(const f32x4*)(base + off + bj * HALF + 4) + acc[ai][bj][m][1];
;                     { u32x4 xw; xw.x = cvt_pk_bf16(v0[0], v0[1]); xw.y = cvt_pk_bf16(v0[2], v0[3]); xw.z = cvt_pk_bf16(v1[0], v1[1]); xw.w = cvt_pk_bf16(v1[2], v1[3]); *(u32x4*)(C + off + bj * HALF) = xw; }
;                     const f32x4 h0 = v0 * gv[bj][0], h1 = v1 * gv[bj][1];
;                     u32x2 w; w.x = cvt_pk4_fp8(h0[0], h0[1], h0[2], h0[3]); w.y = cvt_pk4_fp8(h1[0], h1[1], h1[2], h1[3]);
;                     *(u32x2*)(H2 + off + bj * HALF) = w; } }
	v_pk_add_f32 v[60:61], v[60:61], v[176:177]
	v_pk_add_f32 v[64:65], v[58:59], v[182:183]
	v_pk_add_f32 v[58:59], v[56:57], v[180:181]
	v_pk_add_f32 v[62:63], v[62:63], v[178:179]
	v_add_u32_e32 v233, 0x160000, v232
	global_load_dwordx4 v[176:179], v233, s[6:7] offset:512 nt
	global_load_dwordx4 v[180:183], v233, s[6:7] offset:528 nt
	v_cvt_pk_bf16_f32 v56, v60, v61
	v_pk_mul_f32 v[60:61], v[116:117], v[60:61]
	v_pk_mul_f32 v[66:67], v[112:113], v[58:59]
	v_cvt_pk_fp8_f32 v72, v60, v61
	v_cvt_pk_fp8_f32 v73, v66, v67
	v_cvt_pk_bf16_f32 v57, v62, v63
	v_pk_mul_f32 v[60:61], v[118:119], v[62:63]
	v_pk_mul_f32 v[62:63], v[114:115], v[64:65]
	v_cvt_pk_fp8_f32 v72, v60, v61 op_sel:[0,0,1]
	v_cvt_pk_fp8_f32 v73, v62, v63 op_sel:[0,0,1]
	v_cvt_pk_bf16_f32 v58, v58, v59
	v_cvt_pk_bf16_f32 v59, v64, v65
	global_store_dwordx4 v[74:75], v[56:59], off
	global_store_dwordx2 v[76:77], v[72:73], off
	v_lshl_add_u64 v[66:67], v[146:147], 0, s[22:23]
	v_lshl_add_u64 v[68:69], v[66:67], 2, s[6:7]
	s_waitcnt vmcnt(26)
	v_pk_add_f32 v[52:53], v[52:53], v[184:185]
	v_pk_add_f32 v[56:57], v[50:51], v[190:191]
	v_pk_add_f32 v[50:51], v[48:49], v[188:189]
	v_pk_add_f32 v[54:55], v[54:55], v[186:187]
	v_cvt_pk_bf16_f32 v48, v52, v53
	v_pk_mul_f32 v[52:53], v[100:101], v[52:53]
	v_pk_mul_f32 v[58:59], v[96:97], v[50:51]
	v_cvt_pk_fp8_f32 v64, v52, v53
	v_cvt_pk_fp8_f32 v65, v58, v59
	v_cvt_pk_bf16_f32 v49, v54, v55
	v_pk_mul_f32 v[52:53], v[102:103], v[54:55]
	v_pk_mul_f32 v[54:55], v[98:99], v[56:57]
	v_cvt_pk_fp8_f32 v64, v52, v53 op_sel:[0,0,1]
	v_cvt_pk_fp8_f32 v65, v54, v55 op_sel:[0,0,1]
	v_cvt_pk_bf16_f32 v50, v50, v51
	v_cvt_pk_bf16_f32 v51, v56, v57
	global_store_dwordx4 v[74:75], v[48:51], off offset:256
	global_store_dwordx2 v[76:77], v[64:65], off offset:128
	v_lshl_add_u64 v[58:59], v[66:67], 1, s[14:15]
	v_lshl_add_u64 v[60:61], s[10:11], 0, v[66:67]
	s_waitcnt vmcnt(24)
	v_pk_add_f32 v[44:45], v[44:45], v[192:193]
	v_pk_add_f32 v[48:49], v[42:43], v[198:199]
	v_pk_add_f32 v[42:43], v[40:41], v[196:197]
	v_pk_add_f32 v[46:47], v[46:47], v[194:195]
	v_cvt_pk_bf16_f32 v40, v44, v45
	v_pk_mul_f32 v[44:45], v[116:117], v[44:45]
	v_pk_mul_f32 v[50:51], v[112:113], v[42:43]
	v_cvt_pk_fp8_f32 v56, v44, v45
	v_cvt_pk_fp8_f32 v57, v50, v51
	v_cvt_pk_bf16_f32 v41, v46, v47
	v_pk_mul_f32 v[44:45], v[118:119], v[46:47]
	v_pk_mul_f32 v[46:47], v[114:115], v[48:49]
	v_cvt_pk_fp8_f32 v56, v44, v45 op_sel:[0,0,1]
	v_cvt_pk_fp8_f32 v57, v46, v47 op_sel:[0,0,1]
	v_cvt_pk_bf16_f32 v42, v42, v43
	v_cvt_pk_bf16_f32 v43, v48, v49
	global_store_dwordx4 v[58:59], v[40:43], off
	global_store_dwordx2 v[60:61], v[56:57], off
	v_lshl_add_u64 v[50:51], v[146:147], 0, s[24:25]
	v_lshl_add_u64 v[52:53], v[50:51], 2, s[6:7]
	s_waitcnt vmcnt(22)
	v_pk_add_f32 v[36:37], v[36:37], v[200:201]
	v_pk_add_f32 v[40:41], v[34:35], v[206:207]
	v_pk_add_f32 v[34:35], v[32:33], v[204:205]
	v_pk_add_f32 v[38:39], v[38:39], v[202:203]
	v_cvt_pk_bf16_f32 v32, v36, v37
	v_pk_mul_f32 v[36:37], v[100:101], v[36:37]
	v_pk_mul_f32 v[42:43], v[96:97], v[34:35]
	v_cvt_pk_fp8_f32 v48, v36, v37
	v_cvt_pk_fp8_f32 v49, v42, v43
	v_cvt_pk_bf16_f32 v33, v38, v39
	v_pk_mul_f32 v[36:37], v[102:103], v[38:39]
	v_pk_mul_f32 v[38:39], v[98:99], v[40:41]
	v_cvt_pk_fp8_f32 v48, v36, v37 op_sel:[0,0,1]
	v_cvt_pk_fp8_f32 v49, v38, v39 op_sel:[0,0,1]
	v_cvt_pk_bf16_f32 v34, v34, v35
	v_cvt_pk_bf16_f32 v35, v40, v41
	global_store_dwordx4 v[58:59], v[32:35], off offset:256
	global_store_dwordx2 v[60:61], v[48:49], off offset:128
	v_lshl_add_u64 v[42:43], v[50:51], 1, s[14:15]
	v_lshl_add_u64 v[44:45], s[10:11], 0, v[50:51]
	s_waitcnt vmcnt(20)
	v_pk_add_f32 v[28:29], v[28:29], v[208:209]
	v_pk_add_f32 v[32:33], v[26:27], v[214:215]
	v_pk_add_f32 v[26:27], v[24:25], v[212:213]
	v_pk_add_f32 v[30:31], v[30:31], v[210:211]
	v_cvt_pk_bf16_f32 v24, v28, v29
	v_pk_mul_f32 v[28:29], v[116:117], v[28:29]
	v_pk_mul_f32 v[34:35], v[112:113], v[26:27]
	v_cvt_pk_fp8_f32 v40, v28, v29
	v_cvt_pk_fp8_f32 v41, v34, v35
	v_cvt_pk_bf16_f32 v25, v30, v31
	v_pk_mul_f32 v[28:29], v[118:119], v[30:31]
	v_pk_mul_f32 v[30:31], v[114:115], v[32:33]
	v_cvt_pk_fp8_f32 v40, v28, v29 op_sel:[0,0,1]
	v_cvt_pk_fp8_f32 v41, v30, v31 op_sel:[0,0,1]
	v_cvt_pk_bf16_f32 v26, v26, v27
	v_cvt_pk_bf16_f32 v27, v32, v33
	global_store_dwordx4 v[42:43], v[24:27], off
	global_store_dwordx2 v[44:45], v[40:41], off
	v_lshl_add_u64 v[34:35], v[146:147], 0, s[26:27]
	v_lshl_add_u64 v[36:37], v[34:35], 2, s[6:7]
	s_waitcnt vmcnt(18)
	v_pk_add_f32 v[20:21], v[20:21], v[216:217]
	v_pk_add_f32 v[24:25], v[18:19], v[222:223]
	v_pk_add_f32 v[18:19], v[16:17], v[220:221]
	v_pk_add_f32 v[22:23], v[22:23], v[218:219]
	v_cvt_pk_bf16_f32 v16, v20, v21
	v_pk_mul_f32 v[20:21], v[100:101], v[20:21]
	v_pk_mul_f32 v[26:27], v[96:97], v[18:19]
	v_cvt_pk_fp8_f32 v32, v20, v21
	v_cvt_pk_fp8_f32 v33, v26, v27
	v_cvt_pk_bf16_f32 v17, v22, v23
	v_pk_mul_f32 v[20:21], v[102:103], v[22:23]
	v_pk_mul_f32 v[22:23], v[98:99], v[24:25]
	v_cvt_pk_fp8_f32 v32, v20, v21 op_sel:[0,0,1]
	v_cvt_pk_fp8_f32 v33, v22, v23 op_sel:[0,0,1]
	v_cvt_pk_bf16_f32 v18, v18, v19
	v_cvt_pk_bf16_f32 v19, v24, v25
	global_store_dwordx4 v[42:43], v[16:19], off offset:256
	global_store_dwordx2 v[44:45], v[32:33], off offset:128
	v_lshl_add_u64 v[26:27], v[34:35], 1, s[14:15]
	v_lshl_add_u64 v[28:29], s[10:11], 0, v[34:35]
	s_waitcnt vmcnt(16)
	v_pk_add_f32 v[12:13], v[12:13], v[224:225]
	v_pk_add_f32 v[16:17], v[10:11], v[230:231]
	v_pk_add_f32 v[10:11], v[8:9], v[228:229]
	v_pk_add_f32 v[14:15], v[14:15], v[226:227]
	v_cvt_pk_bf16_f32 v8, v12, v13
	v_pk_mul_f32 v[12:13], v[116:117], v[12:13]
	v_pk_mul_f32 v[18:19], v[112:113], v[10:11]
	v_cvt_pk_fp8_f32 v24, v12, v13
	v_cvt_pk_fp8_f32 v25, v18, v19
	v_cvt_pk_bf16_f32 v9, v14, v15
	v_pk_mul_f32 v[12:13], v[118:119], v[14:15]
	v_pk_mul_f32 v[14:15], v[114:115], v[16:17]
	v_cvt_pk_fp8_f32 v24, v12, v13 op_sel:[0,0,1]
	v_cvt_pk_fp8_f32 v25, v14, v15 op_sel:[0,0,1]
	v_cvt_pk_bf16_f32 v10, v10, v11
	v_cvt_pk_bf16_f32 v11, v16, v17
	global_store_dwordx4 v[26:27], v[8:11], off
	global_store_dwordx2 v[28:29], v[24:25], off
	s_waitcnt vmcnt(14)
	v_pk_add_f32 v[4:5], v[4:5], v[176:177]
	v_pk_add_f32 v[8:9], v[2:3], v[182:183]
	v_pk_add_f32 v[2:3], v[0:1], v[180:181]
	v_pk_add_f32 v[6:7], v[6:7], v[178:179]
	v_cvt_pk_bf16_f32 v0, v4, v5
	v_pk_mul_f32 v[4:5], v[100:101], v[4:5]
	v_pk_mul_f32 v[10:11], v[96:97], v[2:3]
	v_cvt_pk_fp8_f32 v144, v4, v5
	v_cvt_pk_fp8_f32 v145, v10, v11
	v_cvt_pk_bf16_f32 v1, v6, v7
	v_pk_mul_f32 v[4:5], v[102:103], v[6:7]
	v_pk_mul_f32 v[6:7], v[98:99], v[8:9]
	v_cvt_pk_fp8_f32 v144, v4, v5 op_sel:[0,0,1]
	v_cvt_pk_fp8_f32 v145, v6, v7 op_sel:[0,0,1]
	v_cvt_pk_bf16_f32 v2, v2, v3
	v_cvt_pk_bf16_f32 v3, v8, v9
	global_store_dwordx4 v[26:27], v[0:3], off offset:256
	global_store_dwordx2 v[28:29], v[144:145], off offset:128
	s_cbranch_vccnz .LBB0_910
	s_andn2_b64 vcc, exec, s[16:17]
	s_cbranch_vccnz .LBB0_909
	s_barrier
	s_branch .LBB0_909
